# block selection: importance-key assembly also skipped when the query block has at most 16 valid blocks
# baseline (speedup 1.0000x reference)
; #define LAS __attribute__((address_space(3)))
; #define ATT_WAIT_BAR() asm volatile("s_waitcnt vmcnt(0) lgkmcnt(0)\n\ts_barrier" ::: "memory")
; __device__ __forceinline__ int opq_v(int x) { asm volatile("" : "+v"(x)); return x; }
; __device__ __forceinline__ void att_unit_mfma(KArgs args, int b, int qb, LAS unsigned char* lds, int wave0, int lane0, int tid0) {
;     ...
;         ATT_WAIT_BAR();
;         { ATT_IDS const char* ksb0 = (const char*)(z + (size_t)(b * SEQ) * ZP + ZC_KS + g * 64);
;           const char* kp0 = ksb0 + (size_t)(64 * qb) * ZPB; att_stage(lds, 0, kp0, kp0 + (ZC_VS - ZC_KS) * 2, ZPB, wave, lane);
;           const char* kp1 = ksb0 + (size_t)(64 * (qb > 0 ? qb - 1 : 0)) * ZPB; att_stage(lds, 1, kp1, kp1 + (ZC_VS - ZC_KS) * 2, ZPB, wave, lane); }
;         { const int tid = opq_v(tid0); const int stok = tid >> 3, e8 = tid & 7; const LAS float* ilc = (const LAS float*)(lds + ATT_SC);
;           unsigned key[8];
; #pragma unroll
;           for (int k = 0; k < 8; ++k) { const int j = 8 * e8 + k; const float v = imp[(0 * 64 + stok) * 65 + j] * ilc[stok] + imp[(1 * 64 + stok) * 65 + j] * ilc[64 + stok] + imp[(2 * 64 + stok) * 65 + j] * ilc[128 + stok] + imp[(3 * 64 + stok) * 65 + j] * ilc[192 + stok];
;               const bool valid = j <= qb, forced = valid && (j == 0 || j == qb || j == qb - 1);
;               const unsigned bits_ = __builtin_bit_cast(unsigned, forced ? 1e30f : (valid ? v : -1e30f));
;               key[k] = ((bits_ ^ ((bits_ >> 31) ? 0xFFFFFFFFu : 0x80000000u)) & ~63u) | (unsigned)(63 - j); }
;           unsigned T = 0u;
.LBB0_590:
	s_lshl_b32 s0, s36, 6
	s_xor_b64 s[16:17], s[48:49], -1
	v_mov_b32_e32 v1, v174
	s_lshl_b32 s0, s0, 1
	v_readlane_b32 s1, v255, 26
	s_waitcnt vmcnt(0) lgkmcnt(0)
	s_barrier
	s_mov_b32 s4, s69
	s_add_u32 s70, s1, s0
	v_readlane_b32 s0, v255, 28
	v_ashrrev_i32_e32 v8, 3, v1
	s_addc_u32 s71, s0, 0
	s_mul_i32 s0, s2, 0x50000
	v_lshl_add_u32 v10, s4, 3, v8
	s_add_u32 s0, s70, s0
	s_mul_hi_i32 s1, s3, 0x1400
	v_lshrrev_b32_e32 v4, 1, v10
	s_addc_u32 s1, s71, s1
	v_and_b32_e32 v9, 7, v1
	v_xor_b32_e32 v1, v4, v1
	v_mov_b64_e32 v[2:3], s[0:1]
	v_lshlrev_b32_e32 v1, 4, v1
	v_mad_i64_i32 v[2:3], s[0:1], v10, s88, v[2:3]
	v_and_b32_e32 v4, 0x70, v1
	v_lshlrev_b32_e32 v1, 1, v8
	v_mov_b32_e32 v5, v0
	v_bitop3_b32 v1, v1, v9, 6 bitop3:0x6c
	s_lshl_b32 s0, s4, 10
	s_waitcnt vmcnt(0)
	v_lshl_add_u64 v[6:7], v[2:3], 0, v[4:5]
	s_mov_b64 s[6:7], 0xe00
	v_lshlrev_b32_e32 v8, 4, v1
	v_mov_b32_e32 v9, v0
	s_add_i32 s4, s0, 0
	v_lshl_add_u64 v[6:7], v[6:7], 0, s[6:7]
	v_lshl_add_u64 v[2:3], v[2:3], 0, v[8:9]
	s_mov_b64 s[8:9], 0xf00
	s_add_i32 s0, s4, 0x2000
	s_mov_b32 s1, m0
	s_mov_b32 m0, s4
	s_nop 0
	global_load_lds_dwordx4 v[6:7], off
	s_mov_b32 m0, s1
	v_lshl_add_u64 v[2:3], v[2:3], 0, s[8:9]
	s_mov_b32 s1, m0
	s_mov_b32 m0, s0
	s_nop 0
	global_load_lds_dwordx4 v[2:3], off
	s_mov_b32 m0, s1
	v_readlane_b32 s0, v255, 52
	s_add_u32 s0, s70, s0
	v_readlane_b32 s1, v255, 51
	s_addc_u32 s1, s71, s1
	v_mov_b32_e32 v1, v175
	v_mov_b64_e32 v[2:3], s[0:1]
	v_mad_i64_i32 v[2:3], s[0:1], v10, s88, v[2:3]
	v_lshl_add_u64 v[4:5], v[2:3], 0, v[4:5]
	v_lshl_add_u64 v[4:5], v[4:5], 0, s[6:7]
	v_lshl_add_u64 v[2:3], v[2:3], 0, v[8:9]
	s_add_i32 s0, s4, 0x4000
	s_mov_b32 s1, m0
	s_mov_b32 m0, s0
	s_nop 0
	global_load_lds_dwordx4 v[4:5], off
	s_mov_b32 m0, s1
	v_lshl_add_u64 v[2:3], v[2:3], 0, s[8:9]
	s_addk_i32 s4, 0x6000
	s_mov_b32 s0, m0
	s_mov_b32 m0, s4
	s_nop 0
	global_load_lds_dwordx4 v[2:3], off
	s_mov_b32 m0, s0
	s_mov_b64 s[80:81], 0xe00
	v_ashrrev_i32_e32 v4, 3, v1
	v_and_b32_e32 v2, 7, v1
	v_mul_lo_u32 v5, v4, s56
	v_lshlrev_b32_e32 v3, 3, v2
	v_add_u32_e32 v11, s37, v5
	v_lshl_add_u32 v7, v4, 2, s91
	s_mov_b64 s[96:97], 0xf00
	v_add_u32_e32 v12, 0x4100, v11
	v_add_u32_e32 v8, 0x100, v7
	v_add_u32_e32 v13, 0x8200, v11
	v_add_u32_e32 v5, 0x200, v7
	v_add_u32_e32 v16, 0xc300, v11
	v_add_u32_e32 v6, 0x300, v7
	v_cmp_ge_i32_e32 vcc, s2, v3
	v_mov_b32_e32 v4, 0xf149f2ca
	v_lshlrev_b32_e32 v17, 2, v3
	v_mov_b32_e32 v9, 0xf149f2ca
	s_cmp_lt_i32 s2, 16
	s_cbranch_scc1 .LBB0_606
	s_and_saveexec_b64 s[6:7], vcc
	s_cbranch_execz .LBB0_592
	v_add_u32_e32 v9, v11, v17
	ds_read_b32 v14, v9
	ds_read_b32 v18, v7
	v_add_u32_e32 v9, v12, v17
	ds_read_b32 v15, v9
	ds_read_b32 v19, v8
	v_add_u32_e32 v9, v13, v17
	v_cmp_eq_u32_e32 vcc, 0, v2
	v_cmp_eq_u32_e64 s[4:5], s2, v3
	s_or_b64 s[0:1], vcc, s[4:5]
	s_waitcnt lgkmcnt(0)
	v_mul_f32_e32 v10, v15, v19
	v_pk_fma_f32 v[14:15], v[14:15], v[18:19], v[10:11] op_sel_hi:[1,1,0]
	ds_read_b32 v18, v9
	ds_read_b32 v20, v5
	v_add_u32_e32 v9, v16, v17
	ds_read_b32 v19, v9
	ds_read_b32 v21, v6
	v_cmp_eq_u32_e32 vcc, s46, v3
	s_or_b64 vcc, s[0:1], vcc
	s_waitcnt lgkmcnt(0)
	v_pk_fma_f32 v[14:15], v[18:19], v[20:21], v[14:15]
	v_mul_f32_e32 v10, v19, v21
	v_pk_add_f32 v[14:15], v[14:15], v[10:11] op_sel_hi:[1,0]
	s_nop 0
	v_cndmask_b32_e32 v9, v14, v214, vcc
